# k_iter first: feats->f16 gather issued before phase 1, convert+store before 2nd barrier (was a serial tail)
# speedup vs baseline: 1.0237x; 1.0132x over previous
.LBB2_21:
	s_load_dwordx2 s[20:21], s[0:1], 0x58
	s_lshl_b32 s66, s27, 3
	s_add_i32 s66, s59, s66
	s_mov_b32 s67, 0
	s_lshl_b64 s[66:67], s[66:67], 2
	s_add_u32 s66, s28, s66
	s_addc_u32 s67, s29, s67
	s_load_dwordx8 s[68:75], s[66:67], 0x0
	v_readfirstlane_b32 s38, v6
	v_cmp_eq_u32_e64 s[14:15], 0, v0
	s_and_saveexec_b64 s[0:1], s[14:15]
	s_cbranch_execz .LBB2_23
	s_lshl_b32 s2, s46, 2
	v_mov_b32_e32 v1, s2
	v_mov_b32_e32 v5, s38
	global_store_dword v1, v5, s[50:51]
	v_mov_b32_e32 v5, s60
	global_store_dword v1, v5, s[48:49]

.LBB2_25:
	s_or_b64 exec, exec, s[0:1]
	s_xor_b32 s0, s16, 0xff
	s_add_i32 s0, s0, s38
	s_ashr_i32 s0, s0, 8
	v_med3_i32 v7, s0, 0, 6
	v_max_f32_e32 v4, v4, v4
	v_readfirstlane_b32 s39, v7
	v_cndmask_b32_e64 v7, v37, v36, s[18:19]
	v_mul_f32_e32 v9, 0x439044f5, v7
	v_max_f32_e32 v4, 0xc6ea6000, v4
	s_waitcnt lgkmcnt(0)
	v_lshlrev_b32_e32 v208, 2, v44
	s_add_i32 s76, s68, s58
	s_lshl_b32 s76, s76, 8
	s_add_u32 s76, s20, s76
	s_addc_u32 s77, s21, 0
	s_add_i32 s78, s69, s58
	s_lshl_b32 s78, s78, 8
	s_add_u32 s78, s20, s78
	s_addc_u32 s79, s21, 0
	s_add_i32 s80, s70, s58
	s_lshl_b32 s80, s80, 8
	s_add_u32 s80, s20, s80
	s_addc_u32 s81, s21, 0
	s_add_i32 s82, s71, s58
	s_lshl_b32 s82, s82, 8
	s_add_u32 s82, s20, s82
	s_addc_u32 s83, s21, 0
	s_add_i32 s84, s72, s58
	s_lshl_b32 s84, s84, 8
	s_add_u32 s84, s20, s84
	s_addc_u32 s85, s21, 0
	s_add_i32 s86, s73, s58
	s_lshl_b32 s86, s86, 8
	s_add_u32 s86, s20, s86
	s_addc_u32 s87, s21, 0
	s_add_i32 s88, s74, s58
	s_lshl_b32 s88, s88, 8
	s_add_u32 s88, s20, s88
	s_addc_u32 s89, s21, 0
	s_add_i32 s90, s75, s58
	s_lshl_b32 s90, s90, 8
	s_add_u32 s90, s20, s90
	s_addc_u32 s91, s21, 0
	global_load_dword v200, v208, s[76:77]
	global_load_dword v201, v208, s[78:79]
	global_load_dword v202, v208, s[80:81]
	global_load_dword v203, v208, s[82:83]
	global_load_dword v204, v208, s[84:85]
	global_load_dword v205, v208, s[86:87]
	global_load_dword v206, v208, s[88:89]
	global_load_dword v207, v208, s[90:91]
	v_cndmask_b32_e64 v1, v11, v10, s[18:19]
	v_cndmask_b32_e64 v4, v4, 1.0, s[18:19]
	v_and_b32_e32 v10, 0xffff0000, v9
	s_mov_b32 s0, 0x439044f5
	v_or_b32_sdwa v40, v9, v10 dst_sel:DWORD dst_unused:UNUSED_PAD src0_sel:WORD_1 src1_sel:DWORD
	v_and_b32_e32 v9, 0xffff0000, v4
	v_mov_b32_e32 v5, 0xff800000
	v_cndmask_b32_e64 v2, v3, v2, s[18:19]
	v_fma_f32 v7, v7, s0, -v10
	v_sub_f32_e32 v10, v4, v9
	v_or_b32_sdwa v42, v4, v9 dst_sel:DWORD dst_unused:UNUSED_PAD src0_sel:WORD_1 src1_sel:DWORD
	v_max_f32_e32 v4, v8, v8
	v_cndmask_b32_e32 v6, v5, v12, vcc
	v_mul_f32_e32 v3, 0x439044f5, v2
	v_max_f32_e32 v4, 0xc6ea6000, v4
	v_cndmask_b32_e64 v115, 1.0, v6, s[18:19]
	v_cndmask_b32_e64 v6, v5, v18, s[2:3]
	v_or_b32_sdwa v41, v7, v9 dst_sel:DWORD dst_unused:UNUSED_PAD src0_sel:WORD_1 src1_sel:DWORD
	v_cndmask_b32_e64 v4, v4, 1.0, s[18:19]
	v_and_b32_e32 v7, 0xffff0000, v3
	v_cndmask_b32_e64 v100, 1.0, v6, s[18:19]
	v_cndmask_b32_e64 v6, v5, v22, s[4:5]
	v_or_b32_sdwa v36, v3, v7 dst_sel:DWORD dst_unused:UNUSED_PAD src0_sel:WORD_1 src1_sel:DWORD
	v_and_b32_e32 v3, 0xffff0000, v4
	v_cndmask_b32_e64 v72, 1.0, v6, s[18:19]
	v_cndmask_b32_e64 v6, v5, v26, s[6:7]
	v_fma_f32 v2, v2, s0, -v7
	v_sub_f32_e32 v7, v4, v3
	v_cndmask_b32_e64 v76, 1.0, v6, s[18:19]
	v_cndmask_b32_e64 v6, v5, v30, s[10:11]
	v_and_b32_e32 v11, 0xffff0000, v10
	v_and_b32_e32 v8, 0xffff0000, v7
	v_cndmask_b32_e64 v50, 1.0, v6, s[18:19]
	v_cndmask_b32_e64 v6, v5, v34, s[12:13]
	s_mov_b32 s1, 0xffff0000
	v_sub_f32_e32 v11, v10, v11
	v_lshrrev_b32_e32 v10, 16, v10
	v_sub_f32_e32 v8, v7, v8
	v_lshrrev_b32_e32 v7, 16, v7
	v_cndmask_b32_e64 v99, v17, v16, s[18:19]
	v_cndmask_b32_e64 v21, v21, v20, s[18:19]
	v_cndmask_b32_e64 v73, v25, v24, s[18:19]
	v_cndmask_b32_e64 v48, v29, v28, s[18:19]
	v_cndmask_b32_e64 v5, v33, v32, s[18:19]
	v_cndmask_b32_e64 v6, 1.0, v6, s[18:19]
	v_and_or_b32 v43, v11, s1, v10
	v_or_b32_sdwa v38, v4, v3 dst_sel:DWORD dst_unused:UNUSED_PAD src0_sel:WORD_1 src1_sel:DWORD
	v_or_b32_sdwa v37, v2, v3 dst_sel:DWORD dst_unused:UNUSED_PAD src0_sel:WORD_1 src1_sel:DWORD
	v_and_or_b32 v39, v8, s1, v7
	s_cmp_lt_i32 s39, 4
	s_mov_b64 s[0:1], 0
	s_cbranch_scc1 .LBB2_30
	s_cmp_gt_i32 s39, 4
	s_cbranch_scc0 .LBB2_33
	s_cmp_gt_i32 s39, 5
	s_cbranch_scc0 .LBB2_34
	s_cmp_eq_u32 s39, 6
	s_mov_b64 s[16:17], 0
	s_cbranch_scc0 .LBB2_151
	v_and_b32_e32 v2, 0xffff0000, v5
	v_max_f32_e32 v3, v6, v6
	v_sub_f32_e32 v2, v5, v2
	v_max_f32_e32 v3, 0xc6ea6000, v3
	v_and_b32_e32 v4, 0xffff0000, v3
	v_and_b32_e32 v2, 0xffff0000, v2
	v_or_b32_sdwa v78, v2, v5 dst_sel:DWORD dst_unused:UNUSED_PAD src0_sel:DWORD src1_sel:WORD_1
	v_sub_f32_e32 v2, v3, v4
	v_or_b32_sdwa v79, v4, v5 dst_sel:DWORD dst_unused:UNUSED_PAD src0_sel:DWORD src1_sel:WORD_1
	v_and_b32_e32 v5, 0xffff0000, v2
	s_mov_b32 s22, 0xffff0000
	v_sub_f32_e32 v5, v2, v5
	v_lshrrev_b32_e32 v2, 16, v2
	v_and_or_b32 v80, v5, s22, v2
	v_or_b32_sdwa v81, v3, v4 dst_sel:DWORD dst_unused:UNUSED_PAD src0_sel:WORD_1 src1_sel:DWORD
	s_movk_i32 s22, 0xfc00
	s_mov_b64 s[24:25], -1
	v_mfma_f32_32x32x16_bf16 v[2:17], v[40:43], v[78:81], 0
	s_nop 11
	v_cvt_pk_f16_f32 v2, v2, v3
	v_cvt_pk_f16_f32 v3, v4, v5
	v_pk_max_i16 v2, v2, s22 op_sel_hi:[1,0]
	v_pk_max_i16 v3, v3, s22 op_sel_hi:[1,0]
	s_nop 0
	v_exp_f16_e32 v20, v2
	v_exp_f16_e32 v49, v3
	v_exp_f16_sdwa v20, v2 dst_sel:WORD_1 dst_unused:UNUSED_PRESERVE src0_sel:WORD_1
	v_exp_f16_sdwa v49, v3 dst_sel:WORD_1 dst_unused:UNUSED_PRESERVE src0_sel:WORD_1
	v_cvt_pk_f16_f32 v2, v6, v7
	v_cvt_pk_f16_f32 v3, v8, v9
	v_pk_max_i16 v2, v2, s22 op_sel_hi:[1,0]
	v_pk_max_i16 v3, v3, s22 op_sel_hi:[1,0]
	s_nop 0
	v_exp_f16_e32 v54, v2
	v_exp_f16_e32 v57, v3
	v_exp_f16_sdwa v54, v2 dst_sel:WORD_1 dst_unused:UNUSED_PRESERVE src0_sel:WORD_1
	v_exp_f16_sdwa v57, v3 dst_sel:WORD_1 dst_unused:UNUSED_PRESERVE src0_sel:WORD_1
	v_cvt_pk_f16_f32 v2, v10, v11
	v_cvt_pk_f16_f32 v3, v12, v13
	v_pk_max_i16 v2, v2, s22 op_sel_hi:[1,0]
	v_pk_max_i16 v3, v3, s22 op_sel_hi:[1,0]
	s_nop 0
	v_exp_f16_e32 v61, v2
	v_exp_f16_e32 v64, v3
	v_exp_f16_sdwa v61, v2 dst_sel:WORD_1 dst_unused:UNUSED_PRESERVE src0_sel:WORD_1
	v_exp_f16_sdwa v64, v3 dst_sel:WORD_1 dst_unused:UNUSED_PRESERVE src0_sel:WORD_1
	v_cvt_pk_f16_f32 v2, v14, v15
	v_cvt_pk_f16_f32 v3, v16, v17
	v_pk_max_i16 v2, v2, s22 op_sel_hi:[1,0]
	v_pk_max_i16 v3, v3, s22 op_sel_hi:[1,0]
	s_nop 0
	v_exp_f16_e32 v67, v2
	v_exp_f16_e32 v69, v3
	v_exp_f16_sdwa v67, v2 dst_sel:WORD_1 dst_unused:UNUSED_PRESERVE src0_sel:WORD_1
	v_exp_f16_sdwa v69, v3 dst_sel:WORD_1 dst_unused:UNUSED_PRESERVE src0_sel:WORD_1
	v_mfma_f32_32x32x16_bf16 v[2:17], v[36:39], v[78:81], 0
	s_nop 11
	v_cvt_pk_f16_f32 v2, v2, v3
	v_cvt_pk_f16_f32 v3, v4, v5
	v_pk_max_i16 v2, v2, s22 op_sel_hi:[1,0]
	v_pk_max_i16 v3, v3, s22 op_sel_hi:[1,0]
	s_nop 0
	v_exp_f16_e32 v75, v2
	v_exp_f16_e32 v79, v3
	v_exp_f16_sdwa v75, v2 dst_sel:WORD_1 dst_unused:UNUSED_PRESERVE src0_sel:WORD_1
	v_exp_f16_sdwa v79, v3 dst_sel:WORD_1 dst_unused:UNUSED_PRESERVE src0_sel:WORD_1
	v_cvt_pk_f16_f32 v2, v6, v7
	v_cvt_pk_f16_f32 v3, v8, v9
	v_pk_max_i16 v2, v2, s22 op_sel_hi:[1,0]
	v_pk_max_i16 v3, v3, s22 op_sel_hi:[1,0]
	s_nop 0
	v_exp_f16_e32 v85, v2
	v_exp_f16_e32 v88, v3
	v_exp_f16_sdwa v85, v2 dst_sel:WORD_1 dst_unused:UNUSED_PRESERVE src0_sel:WORD_1
	v_exp_f16_sdwa v88, v3 dst_sel:WORD_1 dst_unused:UNUSED_PRESERVE src0_sel:WORD_1
	v_cvt_pk_f16_f32 v2, v10, v11
	v_cvt_pk_f16_f32 v3, v12, v13
	v_pk_max_i16 v2, v2, s22 op_sel_hi:[1,0]
	v_pk_max_i16 v3, v3, s22 op_sel_hi:[1,0]
	s_nop 0
	v_exp_f16_e32 v91, v2
	v_exp_f16_e32 v94, v3
	v_exp_f16_sdwa v91, v2 dst_sel:WORD_1 dst_unused:UNUSED_PRESERVE src0_sel:WORD_1
	v_exp_f16_sdwa v94, v3 dst_sel:WORD_1 dst_unused:UNUSED_PRESERVE src0_sel:WORD_1
	v_cvt_pk_f16_f32 v2, v14, v15
	v_cvt_pk_f16_f32 v3, v16, v17
	v_pk_max_i16 v2, v2, s22 op_sel_hi:[1,0]
	v_pk_max_i16 v3, v3, s22 op_sel_hi:[1,0]
	s_nop 0
	v_exp_f16_e32 v97, v2
	v_exp_f16_e32 v98, v3
	v_exp_f16_sdwa v97, v2 dst_sel:WORD_1 dst_unused:UNUSED_PRESERVE src0_sel:WORD_1
	v_exp_f16_sdwa v98, v3 dst_sel:WORD_1 dst_unused:UNUSED_PRESERVE src0_sel:WORD_1
	s_and_b64 vcc, exec, s[16:17]
	s_cbranch_vccnz .LBB2_35
	s_branch .LBB2_36

.LBB2_99:
	s_or_b64 exec, exec, s[22:23]
	s_lshr_b32 s66, s33, 3
	s_or_b32 s66, s66, s26
	s_add_i32 s66, s66, s27
	s_mov_b32 s67, 0
	s_lshl_b64 s[66:67], s[66:67], 10
	s_add_u32 s66, s30, s66
	s_addc_u32 s67, s31, s67
	v_lshlrev_b32_e32 v208, 4, v44
	s_waitcnt vmcnt(0)
	v_cvt_pk_f16_f32 v210, v200, v201
	v_cvt_pk_f16_f32 v211, v202, v203
	v_cvt_pk_f16_f32 v212, v204, v205
	v_cvt_pk_f16_f32 v213, v206, v207
	global_store_dwordx4 v208, v[210:213], s[66:67]
	s_andn2_b64 vcc, exec, s[0:1]
	s_waitcnt lgkmcnt(0)
	s_barrier
	s_cbranch_vccnz .LBB2_117
	v_lshlrev_b32_e32 v0, 3, v1
	v_add_u32_e32 v0, 0x7000, v0
	ds_read2_b64 v[12:15], v0 offset0:196 offset1:198
	ds_read2_b64 v[8:11], v0 offset0:200 offset1:202
	ds_read2_b64 v[4:7], v0 offset0:204 offset1:206
	ds_read2_b64 v[0:3], v0 offset0:208 offset1:210
	v_mov_b32_e32 v21, 0
	ds_read_b32 v36, v21 offset:30368
	s_cmp_lt_i32 s39, 4
	s_mov_b64 s[0:1], 0
	s_cbranch_scc1 .LBB2_118
	s_cmp_gt_i32 s39, 4
	s_cbranch_scc0 .LBB2_119
	s_cmp_gt_i32 s39, 5
	s_cbranch_scc0 .LBB2_129
	s_mov_b64 s[8:9], 0
	s_cmp_eq_u32 s39, 6
	s_mov_b64 s[14:15], 0
	s_cbranch_scc0 .LBB2_107
	v_mov_b32_e32 v37, 0
	s_waitcnt lgkmcnt(4)
	v_dot2c_f32_f16_e32 v37, v20, v12
	v_mov_b32_e32 v20, 0
	v_dot2c_f32_f16_e32 v20, v49, v13
	v_dot2c_f32_f16_e32 v37, v54, v14
	v_dot2c_f32_f16_e32 v20, v57, v15
	s_waitcnt lgkmcnt(3)
	v_dot2c_f32_f16_e32 v37, v61, v8
	v_dot2c_f32_f16_e32 v20, v64, v9
	v_dot2c_f32_f16_e32 v37, v67, v10
	v_dot2c_f32_f16_e32 v20, v69, v11
	s_waitcnt lgkmcnt(2)
	v_dot2c_f32_f16_e32 v37, v75, v4
	v_dot2c_f32_f16_e32 v20, v79, v5
	v_dot2c_f32_f16_e32 v37, v85, v6
	v_dot2c_f32_f16_e32 v20, v88, v7
	s_waitcnt lgkmcnt(1)
	v_dot2c_f32_f16_e32 v37, v91, v0
	v_dot2c_f32_f16_e32 v20, v94, v1
	v_dot2c_f32_f16_e32 v37, v97, v2
	v_dot2c_f32_f16_e32 v20, v98, v3
	s_and_b64 vcc, s[18:19], s[12:13]
	v_cndmask_b32_e32 v35, -1, v35, vcc
	v_mov_b32_e32 v21, 0
	v_add_f32_e32 v20, v37, v20
	v_mov_b32_e32 v37, v20
	s_nop 1
	v_permlane32_swap_b32_e32 v20, v37
	v_cmp_lt_i32_e32 vcc, -1, v35
	s_and_saveexec_b64 s[12:13], vcc
	s_cbranch_execz .LBB2_106
	v_add_f32_e32 v20, v20, v37
	s_waitcnt lgkmcnt(0)
	v_mul_f32_e32 v37, v36, v20
	v_add_u32_e32 v20, s58, v35
	v_lshl_add_u64 v[20:21], v[20:21], 2, s[34:35]
	global_atomic_add_f32 v[20:21], v37, off

.LBB2_150:
	s_or_b64 exec, exec, s[0:1]
	s_endpgm

	.amdhsa_kernel _Z6k_iterILb1ELb0EEvPKfS1_PKiPK15HIP_vector_typeIfLj4EES7_S1_S1_S3_S1_PfS8_S1_S3_PDF16_PS5_SA_PiSA_SB_
		.amdhsa_group_segment_fixed_size 30384
		.amdhsa_private_segment_fixed_size 0
		.amdhsa_kernarg_size 152
		.amdhsa_user_sgpr_count 2
		.amdhsa_user_sgpr_dispatch_ptr 0
		.amdhsa_user_sgpr_queue_ptr 0
		.amdhsa_user_sgpr_kernarg_segment_ptr 1
		.amdhsa_user_sgpr_dispatch_id 0
		.amdhsa_user_sgpr_kernarg_preload_length 0
		.amdhsa_user_sgpr_kernarg_preload_offset 0
		.amdhsa_user_sgpr_private_segment_size 0
		.amdhsa_uses_dynamic_stack 0
		.amdhsa_enable_private_segment 0
		.amdhsa_system_sgpr_workgroup_id_x 1
		.amdhsa_system_sgpr_workgroup_id_y 0
		.amdhsa_system_sgpr_workgroup_id_z 0
		.amdhsa_system_sgpr_workgroup_info 0
		.amdhsa_system_vgpr_workitem_id 0
		.amdhsa_next_free_vgpr 216
		.amdhsa_next_free_sgpr 92
		.amdhsa_accum_offset 216
		.amdhsa_reserve_vcc 1
		.amdhsa_float_round_mode_32 0
		.amdhsa_float_round_mode_16_64 0
		.amdhsa_float_denorm_mode_32 3
		.amdhsa_float_denorm_mode_16_64 3
		.amdhsa_dx10_clamp 1
		.amdhsa_ieee_mode 1
		.amdhsa_fp16_overflow 0
		.amdhsa_tg_split 0
		.amdhsa_exception_fp_ieee_invalid_op 0
		.amdhsa_exception_fp_denorm_src 0
		.amdhsa_exception_fp_ieee_div_zero 0
		.amdhsa_exception_fp_ieee_overflow 0
		.amdhsa_exception_fp_ieee_underflow 0
		.amdhsa_exception_fp_ieee_inexact 0
		.amdhsa_exception_int_div_zero 0
	.end_amdhsa_kernel

amdhsa.kernels:
  - .agpr_count:     0
    .args:
      - .actual_access:  read_only
        .address_space:  global
        .offset:         0
        .size:           8
        .value_kind:     global_buffer
      - .actual_access:  read_only
        .address_space:  global
        .offset:         8
        .size:           8
        .value_kind:     global_buffer
      - .actual_access:  read_only
        .address_space:  global
        .offset:         16
        .size:           8
        .value_kind:     global_buffer
      - .actual_access:  read_only
        .address_space:  global
        .offset:         24
        .size:           8
        .value_kind:     global_buffer
      - .actual_access:  write_only
        .address_space:  global
        .offset:         32
        .size:           8
        .value_kind:     global_buffer
      - .actual_access:  write_only
        .address_space:  global
        .offset:         40
        .size:           8
        .value_kind:     global_buffer
      - .actual_access:  write_only
        .address_space:  global
        .offset:         48
        .size:           8
        .value_kind:     global_buffer
      - .actual_access:  write_only
        .address_space:  global
        .offset:         56
        .size:           8
        .value_kind:     global_buffer
      - .actual_access:  write_only
        .address_space:  global
        .offset:         64
        .size:           8
        .value_kind:     global_buffer
      - .actual_access:  write_only
        .address_space:  global
        .offset:         72
        .size:           8
        .value_kind:     global_buffer
      - .actual_access:  write_only
        .address_space:  global
        .offset:         80
        .size:           8
        .value_kind:     global_buffer
      - .actual_access:  write_only
        .address_space:  global
        .offset:         88
        .size:           8
        .value_kind:     global_buffer
      - .actual_access:  write_only
        .address_space:  global
        .offset:         96
        .size:           8
        .value_kind:     global_buffer
      - .actual_access:  write_only
        .address_space:  global
        .offset:         104
        .size:           8
        .value_kind:     global_buffer
      - .actual_access:  write_only
        .address_space:  global
        .offset:         112
        .size:           8
        .value_kind:     global_buffer
    .group_segment_fixed_size: 67584
    .kernarg_segment_align: 8
    .kernarg_segment_size: 120
    .language:       OpenCL C
    .language_version:
      - 2
      - 0
    .max_flat_workgroup_size: 1024
    .name:           _Z6k_sortPKfS0_PKiS2_PiP15HIP_vector_typeIfLj4EEPfS7_S3_S7_S7_S3_S3_S6_S6_
    .private_segment_fixed_size: 0
    .sgpr_count:     35
    .sgpr_spill_count: 0
    .symbol:         _Z6k_sortPKfS0_PKiS2_PiP15HIP_vector_typeIfLj4EEPfS7_S3_S7_S7_S3_S3_S6_S6_.kd
    .uniform_work_group_size: 1
    .uses_dynamic_stack: false
    .vgpr_count:     40
    .vgpr_spill_count: 0
    .wavefront_size: 64
  - .agpr_count:     0
    .args:
      - .actual_access:  read_only
        .address_space:  global
        .offset:         0
        .size:           8
        .value_kind:     global_buffer
      - .actual_access:  read_only
        .address_space:  global
        .offset:         8
        .size:           8
        .value_kind:     global_buffer
      - .actual_access:  read_only
        .address_space:  global
        .offset:         16
        .size:           8
        .value_kind:     global_buffer
      - .actual_access:  read_only
        .address_space:  global
        .offset:         24
        .size:           8
        .value_kind:     global_buffer
      - .actual_access:  read_only
        .address_space:  global
        .offset:         32
        .size:           8
        .value_kind:     global_buffer
      - .actual_access:  read_only
        .address_space:  global
        .offset:         40
        .size:           8
        .value_kind:     global_buffer
      - .actual_access:  read_only
        .address_space:  global
        .offset:         48
        .size:           8
        .value_kind:     global_buffer
      - .actual_access:  write_only
        .address_space:  global
        .offset:         56
        .size:           8
        .value_kind:     global_buffer
    .group_segment_fixed_size: 145952
    .kernarg_segment_align: 8
    .kernarg_segment_size: 64
    .language:       OpenCL C
    .language_version:
      - 2
      - 0
    .max_flat_workgroup_size: 512
    .name:           _Z7k_finalPK15HIP_vector_typeIfLj4EES2_PKiS4_PKfS6_PKDF16_Pf
    .private_segment_fixed_size: 0
    .sgpr_count:     34
    .sgpr_spill_count: 0
    .symbol:         _Z7k_finalPK15HIP_vector_typeIfLj4EES2_PKiS4_PKfS6_PKDF16_Pf.kd
    .uniform_work_group_size: 1
    .uses_dynamic_stack: false
    .vgpr_count:     177
    .vgpr_spill_count: 0
    .wavefront_size: 64
  - .agpr_count:     0
    .args:
      - .actual_access:  read_only
        .address_space:  global
        .offset:         0
        .size:           8
        .value_kind:     global_buffer
      - .actual_access:  read_only
        .address_space:  global
        .offset:         8
        .size:           8
        .value_kind:     global_buffer
      - .actual_access:  read_only
        .address_space:  global
        .offset:         16
        .size:           8
        .value_kind:     global_buffer
      - .actual_access:  read_only
        .address_space:  global
        .offset:         24
        .size:           8
        .value_kind:     global_buffer
      - .actual_access:  read_only
        .address_space:  global
        .offset:         32
        .size:           8
        .value_kind:     global_buffer
      - .actual_access:  read_only
        .address_space:  global
        .offset:         40
        .size:           8
        .value_kind:     global_buffer
      - .actual_access:  read_only
        .address_space:  global
        .offset:         48
        .size:           8
        .value_kind:     global_buffer
      - .actual_access:  read_only
        .address_space:  global
        .offset:         56
        .size:           8
        .value_kind:     global_buffer
      - .actual_access:  read_only
        .address_space:  global
        .offset:         64
        .size:           8
        .value_kind:     global_buffer
      - .address_space:  global
        .offset:         72
        .size:           8
        .value_kind:     global_buffer
      - .actual_access:  read_only
        .address_space:  global
        .offset:         80
        .size:           8
        .value_kind:     global_buffer
      - .actual_access:  read_only
        .address_space:  global
        .offset:         88
        .size:           8
        .value_kind:     global_buffer
      - .actual_access:  read_only
        .address_space:  global
        .offset:         96
        .size:           8
        .value_kind:     global_buffer
      - .actual_access:  write_only
        .address_space:  global
        .offset:         104
        .size:           8
        .value_kind:     global_buffer
      - .address_space:  global
        .offset:         112
        .size:           8
        .value_kind:     global_buffer
      - .actual_access:  write_only
        .address_space:  global
        .offset:         120
        .size:           8
        .value_kind:     global_buffer
      - .actual_access:  write_only
        .address_space:  global
        .offset:         128
        .size:           8
        .value_kind:     global_buffer
      - .actual_access:  write_only
        .address_space:  global
        .offset:         136
        .size:           8
        .value_kind:     global_buffer
      - .actual_access:  write_only
        .address_space:  global
        .offset:         144
        .size:           8
        .value_kind:     global_buffer
    .group_segment_fixed_size: 30384
    .kernarg_segment_align: 8
    .kernarg_segment_size: 152
    .language:       OpenCL C
    .language_version:
      - 2
      - 0
    .max_flat_workgroup_size: 512
    .name:           _Z6k_iterILb1ELb0EEvPKfS1_PKiPK15HIP_vector_typeIfLj4EES7_S1_S1_S3_S1_PfS8_S1_S3_PDF16_PS5_SA_PiSA_SB_
    .private_segment_fixed_size: 0
    .sgpr_count:     98
    .sgpr_spill_count: 0
    .symbol:         _Z6k_iterILb1ELb0EEvPKfS1_PKiPK15HIP_vector_typeIfLj4EES7_S1_S1_S3_S1_PfS8_S1_S3_PDF16_PS5_SA_PiSA_SB_.kd
    .uniform_work_group_size: 1
    .uses_dynamic_stack: false
    .vgpr_count:     216
    .vgpr_spill_count: 0
    .wavefront_size: 64
  - .agpr_count:     0
    .args:
      - .actual_access:  read_only
        .address_space:  global
        .offset:         0
        .size:           8
        .value_kind:     global_buffer
      - .actual_access:  read_only
        .address_space:  global
        .offset:         8
        .size:           8
        .value_kind:     global_buffer
      - .actual_access:  read_only
        .address_space:  global
        .offset:         16
        .size:           8
        .value_kind:     global_buffer
      - .actual_access:  read_only
        .address_space:  global
        .offset:         24
        .size:           8
        .value_kind:     global_buffer
      - .actual_access:  read_only
        .address_space:  global
        .offset:         32
        .size:           8
        .value_kind:     global_buffer
      - .actual_access:  read_only
        .address_space:  global
        .offset:         40
        .size:           8
        .value_kind:     global_buffer
      - .actual_access:  read_only
        .address_space:  global
        .offset:         48
        .size:           8
        .value_kind:     global_buffer
      - .actual_access:  read_only
        .address_space:  global
        .offset:         56
        .size:           8
        .value_kind:     global_buffer
      - .actual_access:  read_only
        .address_space:  global
        .offset:         64
        .size:           8
        .value_kind:     global_buffer
      - .address_space:  global
        .offset:         72
        .size:           8
        .value_kind:     global_buffer
      - .actual_access:  read_only
        .address_space:  global
        .offset:         80
        .size:           8
        .value_kind:     global_buffer
      - .actual_access:  read_only
        .address_space:  global
        .offset:         88
        .size:           8
        .value_kind:     global_buffer
      - .actual_access:  read_only
        .address_space:  global
        .offset:         96
        .size:           8
        .value_kind:     global_buffer
      - .actual_access:  read_only
        .address_space:  global
        .offset:         104
        .size:           8
        .value_kind:     global_buffer
      - .actual_access:  read_only
        .address_space:  global
        .offset:         112
        .size:           8
        .value_kind:     global_buffer
      - .actual_access:  read_only
        .address_space:  global
        .offset:         120
        .size:           8
        .value_kind:     global_buffer
      - .actual_access:  read_only
        .address_space:  global
        .offset:         128
        .size:           8
        .value_kind:     global_buffer
      - .actual_access:  read_only
        .address_space:  global
        .offset:         136
        .size:           8
        .value_kind:     global_buffer
      - .actual_access:  read_only
        .address_space:  global
        .offset:         144
        .size:           8
        .value_kind:     global_buffer
    .group_segment_fixed_size: 5808
    .kernarg_segment_align: 8
    .kernarg_segment_size: 152
    .language:       OpenCL C
    .language_version:
      - 2
      - 0
    .max_flat_workgroup_size: 512
    .name:           _Z6k_iterILb0ELb0EEvPKfS1_PKiPK15HIP_vector_typeIfLj4EES7_S1_S1_S3_S1_PfS8_S1_S3_PDF16_PS5_SA_PiSA_SB_
    .private_segment_fixed_size: 0
    .sgpr_count:     42
    .sgpr_spill_count: 0
    .symbol:         _Z6k_iterILb0ELb0EEvPKfS1_PKiPK15HIP_vector_typeIfLj4EES7_S1_S1_S3_S1_PfS8_S1_S3_PDF16_PS5_SA_PiSA_SB_.kd
    .uniform_work_group_size: 1
    .uses_dynamic_stack: false
    .vgpr_count:     184
    .vgpr_spill_count: 0
    .wavefront_size: 64
  - .agpr_count:     0
    .args:
      - .actual_access:  read_only
        .address_space:  global
        .offset:         0
        .size:           8
        .value_kind:     global_buffer
      - .actual_access:  read_only
        .address_space:  global
        .offset:         8
        .size:           8
        .value_kind:     global_buffer
      - .actual_access:  read_only
        .address_space:  global
        .offset:         16
        .size:           8
        .value_kind:     global_buffer
      - .actual_access:  read_only
        .address_space:  global
        .offset:         24
        .size:           8
        .value_kind:     global_buffer
      - .actual_access:  read_only
        .address_space:  global
        .offset:         32
        .size:           8
        .value_kind:     global_buffer
      - .actual_access:  read_only
        .address_space:  global
        .offset:         40
        .size:           8
        .value_kind:     global_buffer
      - .actual_access:  read_only
        .address_space:  global
        .offset:         48
        .size:           8
        .value_kind:     global_buffer
      - .actual_access:  read_only
        .address_space:  global
        .offset:         56
        .size:           8
        .value_kind:     global_buffer
      - .actual_access:  read_only
        .address_space:  global
        .offset:         64
        .size:           8
        .value_kind:     global_buffer
      - .address_space:  global
        .offset:         72
        .size:           8
        .value_kind:     global_buffer
      - .actual_access:  write_only
        .address_space:  global
        .offset:         80
        .size:           8
        .value_kind:     global_buffer
      - .actual_access:  read_only
        .address_space:  global
        .offset:         88
        .size:           8
        .value_kind:     global_buffer
      - .actual_access:  read_only
        .address_space:  global
        .offset:         96
        .size:           8
        .value_kind:     global_buffer
      - .actual_access:  read_only
        .address_space:  global
        .offset:         104
        .size:           8
        .value_kind:     global_buffer
      - .actual_access:  read_only
        .address_space:  global
        .offset:         112
        .size:           8
        .value_kind:     global_buffer
      - .actual_access:  read_only
        .address_space:  global
        .offset:         120
        .size:           8
        .value_kind:     global_buffer
      - .actual_access:  read_only
        .address_space:  global
        .offset:         128
        .size:           8
        .value_kind:     global_buffer
      - .actual_access:  read_only
        .address_space:  global
        .offset:         136
        .size:           8
        .value_kind:     global_buffer
      - .actual_access:  read_only
        .address_space:  global
        .offset:         144
        .size:           8
        .value_kind:     global_buffer
    .group_segment_fixed_size: 5808
    .kernarg_segment_align: 8
    .kernarg_segment_size: 152
    .language:       OpenCL C
    .language_version:
      - 2
      - 0
    .max_flat_workgroup_size: 512
    .name:           _Z6k_iterILb0ELb1EEvPKfS1_PKiPK15HIP_vector_typeIfLj4EES7_S1_S1_S3_S1_PfS8_S1_S3_PDF16_PS5_SA_PiSA_SB_
    .private_segment_fixed_size: 0
    .sgpr_count:     42
    .sgpr_spill_count: 0
    .symbol:         _Z6k_iterILb0ELb1EEvPKfS1_PKiPK15HIP_vector_typeIfLj4EES7_S1_S1_S3_S1_PfS8_S1_S3_PDF16_PS5_SA_PiSA_SB_.kd
    .uniform_work_group_size: 1
    .uses_dynamic_stack: false
    .vgpr_count:     184
    .vgpr_spill_count: 0
    .wavefront_size: 64
